# P7 queue grabs converted by a hand-written block with the queue index rotated inside 128-item blocks (2 row blocks x 8 column blocks per grab), on top of the reordered fixed share
# baseline (speedup 1.0000x reference)
.LBB0_1059:
	s_or_b64 exec, exec, s[16:17]
	s_and_b64 vcc, exec, s[4:5]
	s_cbranch_vccnz .LBB0_1051
	v_readlane_b32 s12, v255, 28
	s_add_i32 s16, s26, s12
	s_add_i32 s19, s16, 0
	s_and_b32 s20, s19, 1
	s_lshl_b32 s20, s20, 6
	s_and_b32 s21, s19, 0x7e
	s_lshr_b32 s21, s21, 1
	s_andn2_b32 s19, s19, 0x7f
	s_or_b32 s19, s19, s20
	s_or_b32 s19, s19, s21
	s_add_i32 s17, s19, 0x4000
	s_add_i32 s19, s16, 8
	s_and_b32 s20, s19, 1
	s_lshl_b32 s20, s20, 6
	s_and_b32 s21, s19, 0x7e
	s_lshr_b32 s21, s21, 1
	s_andn2_b32 s19, s19, 0x7f
	s_or_b32 s19, s19, s20
	s_or_b32 s19, s19, s21
	s_add_i32 s18, s19, 0x4000
	v_mbcnt_lo_u32_b32 v154, -1, 0
	v_mbcnt_hi_u32_b32 v154, -1, v154
	v_lshrrev_b32_e32 v155, 3, v154
	v_and_b32_e32 v154, 7, v154
	v_lshlrev_b32_e32 v152, 17, v155
	v_lshl_or_b32 v152, v154, 4, v152
	v_lshlrev_b32_e32 v153, 13, v154
	v_lshl_or_b32 v153, v155, 4, v153
	s_mov_b32 s36, 0x44000000
	s_lshr_b32 s19, s17, 10
	s_and_b32 s20, s17, 0x3ff
	s_lshr_b32 s21, s20, 6
	s_and_b32 s20, s20, 63
	s_lshl_b32 s22, s19, 24
	s_lshl_b32 s27, s21, 20
	s_add_i32 s22, s22, s27
	s_lshl_b32 s27, s20, 7
	s_add_i32 s22, s22, s27
	s_add_u32 s24, s70, s22
	s_addc_u32 s25, s71, 0
	global_load_dwordx4 v[0:3], v152, s[24:25] sc1 nt
	s_add_u32 s28, s24, 0x2000
	s_addc_u32 s29, s25, 0
	global_load_dwordx4 v[4:7], v152, s[28:29] sc1 nt
	s_add_u32 s28, s24, 0x4000
	s_addc_u32 s29, s25, 0
	global_load_dwordx4 v[8:11], v152, s[28:29] sc1 nt
	s_add_u32 s28, s24, 0x6000
	s_addc_u32 s29, s25, 0
	global_load_dwordx4 v[12:15], v152, s[28:29] sc1 nt
	s_add_u32 s28, s24, 0x8000
	s_addc_u32 s29, s25, 0
	global_load_dwordx4 v[16:19], v152, s[28:29] sc1 nt
	s_add_u32 s28, s24, 0xa000
	s_addc_u32 s29, s25, 0
	global_load_dwordx4 v[20:23], v152, s[28:29] sc1 nt
	s_add_u32 s28, s24, 0xc000
	s_addc_u32 s29, s25, 0
	global_load_dwordx4 v[24:27], v152, s[28:29] sc1 nt
	s_add_u32 s28, s24, 0xe000
	s_addc_u32 s29, s25, 0
	global_load_dwordx4 v[28:31], v152, s[28:29] sc1 nt
	s_add_u32 s28, s24, 0x10000
	s_addc_u32 s29, s25, 0
	global_load_dwordx4 v[32:35], v152, s[28:29] sc1 nt
	s_add_u32 s28, s24, 0x12000
	s_addc_u32 s29, s25, 0
	global_load_dwordx4 v[36:39], v152, s[28:29] sc1 nt
	s_add_u32 s28, s24, 0x14000
	s_addc_u32 s29, s25, 0
	global_load_dwordx4 v[40:43], v152, s[28:29] sc1 nt
	s_add_u32 s28, s24, 0x16000
	s_addc_u32 s29, s25, 0
	global_load_dwordx4 v[44:47], v152, s[28:29] sc1 nt
	s_add_u32 s28, s24, 0x18000
	s_addc_u32 s29, s25, 0
	global_load_dwordx4 v[48:51], v152, s[28:29] sc1 nt
	s_add_u32 s28, s24, 0x1a000
	s_addc_u32 s29, s25, 0
	global_load_dwordx4 v[52:55], v152, s[28:29] sc1 nt
	s_add_u32 s28, s24, 0x1c000
	s_addc_u32 s29, s25, 0
	global_load_dwordx4 v[56:59], v152, s[28:29] sc1 nt
	s_add_u32 s28, s24, 0x1e000
	s_addc_u32 s29, s25, 0
	global_load_dwordx4 v[60:63], v152, s[28:29] sc1 nt
	s_lshr_b32 s19, s18, 10
	s_and_b32 s20, s18, 0x3ff
	s_lshr_b32 s21, s20, 6
	s_and_b32 s20, s20, 63
	s_lshl_b32 s22, s19, 24
	s_lshl_b32 s27, s21, 20
	s_add_i32 s22, s22, s27
	s_lshl_b32 s27, s20, 7
	s_add_i32 s22, s22, s27
	s_add_u32 s24, s70, s22
	s_addc_u32 s25, s71, 0
	global_load_dwordx4 v[64:67], v152, s[24:25] sc1 nt
	s_add_u32 s28, s24, 0x2000
	s_addc_u32 s29, s25, 0
	global_load_dwordx4 v[68:71], v152, s[28:29] sc1 nt
	s_add_u32 s28, s24, 0x4000
	s_addc_u32 s29, s25, 0
	global_load_dwordx4 v[72:75], v152, s[28:29] sc1 nt
	s_add_u32 s28, s24, 0x6000
	s_addc_u32 s29, s25, 0
	global_load_dwordx4 v[76:79], v152, s[28:29] sc1 nt
	s_add_u32 s28, s24, 0x8000
	s_addc_u32 s29, s25, 0
	global_load_dwordx4 v[80:83], v152, s[28:29] sc1 nt
	s_add_u32 s28, s24, 0xa000
	s_addc_u32 s29, s25, 0
	global_load_dwordx4 v[84:87], v152, s[28:29] sc1 nt
	s_add_u32 s28, s24, 0xc000
	s_addc_u32 s29, s25, 0
	global_load_dwordx4 v[88:91], v152, s[28:29] sc1 nt
	s_add_u32 s28, s24, 0xe000
	s_addc_u32 s29, s25, 0
	global_load_dwordx4 v[92:95], v152, s[28:29] sc1 nt
	s_add_u32 s28, s24, 0x10000
	s_addc_u32 s29, s25, 0
	global_load_dwordx4 v[96:99], v152, s[28:29] sc1 nt
	s_add_u32 s28, s24, 0x12000
	s_addc_u32 s29, s25, 0
	global_load_dwordx4 v[100:103], v152, s[28:29] sc1 nt
	s_add_u32 s28, s24, 0x14000
	s_addc_u32 s29, s25, 0
	global_load_dwordx4 v[104:107], v152, s[28:29] sc1 nt
	s_add_u32 s28, s24, 0x16000
	s_addc_u32 s29, s25, 0
	global_load_dwordx4 v[108:111], v152, s[28:29] sc1 nt
	s_add_u32 s28, s24, 0x18000
	s_addc_u32 s29, s25, 0
	global_load_dwordx4 v[112:115], v152, s[28:29] sc1 nt
	s_add_u32 s28, s24, 0x1a000
	s_addc_u32 s29, s25, 0
	global_load_dwordx4 v[116:119], v152, s[28:29] sc1 nt
	s_add_u32 s28, s24, 0x1c000
	s_addc_u32 s29, s25, 0
	global_load_dwordx4 v[120:123], v152, s[28:29] sc1 nt
	s_add_u32 s28, s24, 0x1e000
	s_addc_u32 s29, s25, 0
	global_load_dwordx4 v[124:127], v152, s[28:29] sc1 nt
	s_waitcnt vmcnt(16)
	s_lshr_b32 s19, s17, 10
	s_and_b32 s20, s17, 0x3ff
	s_lshr_b32 s21, s20, 6
	s_and_b32 s20, s20, 63
	s_lshl_b32 s22, s19, 22
	s_lshl_b32 s27, s20, 16
	s_add_i32 s22, s22, s27
	s_lshl_b32 s27, s21, 7
	s_add_i32 s22, s22, s27
	s_add_u32 s30, s90, s22
	s_addc_u32 s31, s91, 0
	s_add_u32 s30, s30, 0x3b100000
	s_addc_u32 s31, s31, 0
	s_add_u32 s34, s30, 0x1000
	s_addc_u32 s35, s31, 0
	v_pk_mul_f32 v[0:1], v[0:1], s[36:37] op_sel_hi:[1,0]
	v_pk_mul_f32 v[2:3], v[2:3], s[36:37] op_sel_hi:[1,0]
	v_pk_mul_f32 v[4:5], v[4:5], s[36:37] op_sel_hi:[1,0]
	v_pk_mul_f32 v[6:7], v[6:7], s[36:37] op_sel_hi:[1,0]
	v_pk_mul_f32 v[8:9], v[8:9], s[36:37] op_sel_hi:[1,0]
	v_pk_mul_f32 v[10:11], v[10:11], s[36:37] op_sel_hi:[1,0]
	v_pk_mul_f32 v[12:13], v[12:13], s[36:37] op_sel_hi:[1,0]
	v_pk_mul_f32 v[14:15], v[14:15], s[36:37] op_sel_hi:[1,0]
	v_pk_mul_f32 v[16:17], v[16:17], s[36:37] op_sel_hi:[1,0]
	v_pk_mul_f32 v[18:19], v[18:19], s[36:37] op_sel_hi:[1,0]
	v_pk_mul_f32 v[20:21], v[20:21], s[36:37] op_sel_hi:[1,0]
	v_pk_mul_f32 v[22:23], v[22:23], s[36:37] op_sel_hi:[1,0]
	v_pk_mul_f32 v[24:25], v[24:25], s[36:37] op_sel_hi:[1,0]
	v_pk_mul_f32 v[26:27], v[26:27], s[36:37] op_sel_hi:[1,0]
	v_pk_mul_f32 v[28:29], v[28:29], s[36:37] op_sel_hi:[1,0]
	v_pk_mul_f32 v[30:31], v[30:31], s[36:37] op_sel_hi:[1,0]
	v_pk_mul_f32 v[32:33], v[32:33], s[36:37] op_sel_hi:[1,0]
	v_pk_mul_f32 v[34:35], v[34:35], s[36:37] op_sel_hi:[1,0]
	v_pk_mul_f32 v[36:37], v[36:37], s[36:37] op_sel_hi:[1,0]
	v_pk_mul_f32 v[38:39], v[38:39], s[36:37] op_sel_hi:[1,0]
	v_pk_mul_f32 v[40:41], v[40:41], s[36:37] op_sel_hi:[1,0]
	v_pk_mul_f32 v[42:43], v[42:43], s[36:37] op_sel_hi:[1,0]
	v_pk_mul_f32 v[44:45], v[44:45], s[36:37] op_sel_hi:[1,0]
	v_pk_mul_f32 v[46:47], v[46:47], s[36:37] op_sel_hi:[1,0]
	v_pk_mul_f32 v[48:49], v[48:49], s[36:37] op_sel_hi:[1,0]
	v_pk_mul_f32 v[50:51], v[50:51], s[36:37] op_sel_hi:[1,0]
	v_pk_mul_f32 v[52:53], v[52:53], s[36:37] op_sel_hi:[1,0]
	v_pk_mul_f32 v[54:55], v[54:55], s[36:37] op_sel_hi:[1,0]
	v_pk_mul_f32 v[56:57], v[56:57], s[36:37] op_sel_hi:[1,0]
	v_pk_mul_f32 v[58:59], v[58:59], s[36:37] op_sel_hi:[1,0]
	v_pk_mul_f32 v[60:61], v[60:61], s[36:37] op_sel_hi:[1,0]
	v_pk_mul_f32 v[62:63], v[62:63], s[36:37] op_sel_hi:[1,0]
	v_cvt_pk_fp8_f32 v136, v0, v4
	v_cvt_pk_fp8_f32 v136, v8, v12 op_sel:[0,0,1]
	v_cvt_pk_fp8_f32 v137, v16, v20
	v_cvt_pk_fp8_f32 v137, v24, v28 op_sel:[0,0,1]
	v_cvt_pk_fp8_f32 v138, v32, v36
	v_cvt_pk_fp8_f32 v138, v40, v44 op_sel:[0,0,1]
	v_cvt_pk_fp8_f32 v139, v48, v52
	v_cvt_pk_fp8_f32 v139, v56, v60 op_sel:[0,0,1]
	global_store_dwordx4 v153, v[136:139], s[30:31] sc1
	v_cvt_pk_fp8_f32 v140, v1, v5
	v_cvt_pk_fp8_f32 v140, v9, v13 op_sel:[0,0,1]
	v_cvt_pk_fp8_f32 v141, v17, v21
	v_cvt_pk_fp8_f32 v141, v25, v29 op_sel:[0,0,1]
	v_cvt_pk_fp8_f32 v142, v33, v37
	v_cvt_pk_fp8_f32 v142, v41, v45 op_sel:[0,0,1]
	v_cvt_pk_fp8_f32 v143, v49, v53
	v_cvt_pk_fp8_f32 v143, v57, v61 op_sel:[0,0,1]
	global_store_dwordx4 v153, v[140:143], s[30:31] offset:2048 sc1
	v_cvt_pk_fp8_f32 v144, v2, v6
	v_cvt_pk_fp8_f32 v144, v10, v14 op_sel:[0,0,1]
	v_cvt_pk_fp8_f32 v145, v18, v22
	v_cvt_pk_fp8_f32 v145, v26, v30 op_sel:[0,0,1]
	v_cvt_pk_fp8_f32 v146, v34, v38
	v_cvt_pk_fp8_f32 v146, v42, v46 op_sel:[0,0,1]
	v_cvt_pk_fp8_f32 v147, v50, v54
	v_cvt_pk_fp8_f32 v147, v58, v62 op_sel:[0,0,1]
	global_store_dwordx4 v153, v[144:147], s[34:35] sc1
	v_cvt_pk_fp8_f32 v148, v3, v7
	v_cvt_pk_fp8_f32 v148, v11, v15 op_sel:[0,0,1]
	v_cvt_pk_fp8_f32 v149, v19, v23
	v_cvt_pk_fp8_f32 v149, v27, v31 op_sel:[0,0,1]
	v_cvt_pk_fp8_f32 v150, v35, v39
	v_cvt_pk_fp8_f32 v150, v43, v47 op_sel:[0,0,1]
	v_cvt_pk_fp8_f32 v151, v51, v55
	v_cvt_pk_fp8_f32 v151, v59, v63 op_sel:[0,0,1]
	global_store_dwordx4 v153, v[148:151], s[34:35] offset:2048 sc1
	s_waitcnt vmcnt(4)
	s_lshr_b32 s19, s18, 10
	s_and_b32 s20, s18, 0x3ff
	s_lshr_b32 s21, s20, 6
	s_and_b32 s20, s20, 63
	s_lshl_b32 s22, s19, 22
	s_lshl_b32 s27, s20, 16
	s_add_i32 s22, s22, s27
	s_lshl_b32 s27, s21, 7
	s_add_i32 s22, s22, s27
	s_add_u32 s30, s90, s22
	s_addc_u32 s31, s91, 0
	s_add_u32 s30, s30, 0x3b100000
	s_addc_u32 s31, s31, 0
	s_add_u32 s34, s30, 0x1000
	s_addc_u32 s35, s31, 0
	v_pk_mul_f32 v[64:65], v[64:65], s[36:37] op_sel_hi:[1,0]
	v_pk_mul_f32 v[66:67], v[66:67], s[36:37] op_sel_hi:[1,0]
	v_pk_mul_f32 v[68:69], v[68:69], s[36:37] op_sel_hi:[1,0]
	v_pk_mul_f32 v[70:71], v[70:71], s[36:37] op_sel_hi:[1,0]
	v_pk_mul_f32 v[72:73], v[72:73], s[36:37] op_sel_hi:[1,0]
	v_pk_mul_f32 v[74:75], v[74:75], s[36:37] op_sel_hi:[1,0]
	v_pk_mul_f32 v[76:77], v[76:77], s[36:37] op_sel_hi:[1,0]
	v_pk_mul_f32 v[78:79], v[78:79], s[36:37] op_sel_hi:[1,0]
	v_pk_mul_f32 v[80:81], v[80:81], s[36:37] op_sel_hi:[1,0]
	v_pk_mul_f32 v[82:83], v[82:83], s[36:37] op_sel_hi:[1,0]
	v_pk_mul_f32 v[84:85], v[84:85], s[36:37] op_sel_hi:[1,0]
	v_pk_mul_f32 v[86:87], v[86:87], s[36:37] op_sel_hi:[1,0]
	v_pk_mul_f32 v[88:89], v[88:89], s[36:37] op_sel_hi:[1,0]
	v_pk_mul_f32 v[90:91], v[90:91], s[36:37] op_sel_hi:[1,0]
	v_pk_mul_f32 v[92:93], v[92:93], s[36:37] op_sel_hi:[1,0]
	v_pk_mul_f32 v[94:95], v[94:95], s[36:37] op_sel_hi:[1,0]
	v_pk_mul_f32 v[96:97], v[96:97], s[36:37] op_sel_hi:[1,0]
	v_pk_mul_f32 v[98:99], v[98:99], s[36:37] op_sel_hi:[1,0]
	v_pk_mul_f32 v[100:101], v[100:101], s[36:37] op_sel_hi:[1,0]
	v_pk_mul_f32 v[102:103], v[102:103], s[36:37] op_sel_hi:[1,0]
	v_pk_mul_f32 v[104:105], v[104:105], s[36:37] op_sel_hi:[1,0]
	v_pk_mul_f32 v[106:107], v[106:107], s[36:37] op_sel_hi:[1,0]
	v_pk_mul_f32 v[108:109], v[108:109], s[36:37] op_sel_hi:[1,0]
	v_pk_mul_f32 v[110:111], v[110:111], s[36:37] op_sel_hi:[1,0]
	v_pk_mul_f32 v[112:113], v[112:113], s[36:37] op_sel_hi:[1,0]
	v_pk_mul_f32 v[114:115], v[114:115], s[36:37] op_sel_hi:[1,0]
	v_pk_mul_f32 v[116:117], v[116:117], s[36:37] op_sel_hi:[1,0]
	v_pk_mul_f32 v[118:119], v[118:119], s[36:37] op_sel_hi:[1,0]
	v_pk_mul_f32 v[120:121], v[120:121], s[36:37] op_sel_hi:[1,0]
	v_pk_mul_f32 v[122:123], v[122:123], s[36:37] op_sel_hi:[1,0]
	v_pk_mul_f32 v[124:125], v[124:125], s[36:37] op_sel_hi:[1,0]
	v_pk_mul_f32 v[126:127], v[126:127], s[36:37] op_sel_hi:[1,0]
	v_cvt_pk_fp8_f32 v136, v64, v68
	v_cvt_pk_fp8_f32 v136, v72, v76 op_sel:[0,0,1]
	v_cvt_pk_fp8_f32 v137, v80, v84
	v_cvt_pk_fp8_f32 v137, v88, v92 op_sel:[0,0,1]
	v_cvt_pk_fp8_f32 v138, v96, v100
	v_cvt_pk_fp8_f32 v138, v104, v108 op_sel:[0,0,1]
	v_cvt_pk_fp8_f32 v139, v112, v116
	v_cvt_pk_fp8_f32 v139, v120, v124 op_sel:[0,0,1]
	global_store_dwordx4 v153, v[136:139], s[30:31] sc1
	v_cvt_pk_fp8_f32 v140, v65, v69
	v_cvt_pk_fp8_f32 v140, v73, v77 op_sel:[0,0,1]
	v_cvt_pk_fp8_f32 v141, v81, v85
	v_cvt_pk_fp8_f32 v141, v89, v93 op_sel:[0,0,1]
	v_cvt_pk_fp8_f32 v142, v97, v101
	v_cvt_pk_fp8_f32 v142, v105, v109 op_sel:[0,0,1]
	v_cvt_pk_fp8_f32 v143, v113, v117
	v_cvt_pk_fp8_f32 v143, v121, v125 op_sel:[0,0,1]
	global_store_dwordx4 v153, v[140:143], s[30:31] offset:2048 sc1
	v_cvt_pk_fp8_f32 v144, v66, v70
	v_cvt_pk_fp8_f32 v144, v74, v78 op_sel:[0,0,1]
	v_cvt_pk_fp8_f32 v145, v82, v86
	v_cvt_pk_fp8_f32 v145, v90, v94 op_sel:[0,0,1]
	v_cvt_pk_fp8_f32 v146, v98, v102
	v_cvt_pk_fp8_f32 v146, v106, v110 op_sel:[0,0,1]
	v_cvt_pk_fp8_f32 v147, v114, v118
	v_cvt_pk_fp8_f32 v147, v122, v126 op_sel:[0,0,1]
	global_store_dwordx4 v153, v[144:147], s[34:35] sc1
	v_cvt_pk_fp8_f32 v148, v67, v71
	v_cvt_pk_fp8_f32 v148, v75, v79 op_sel:[0,0,1]
	v_cvt_pk_fp8_f32 v149, v83, v87
	v_cvt_pk_fp8_f32 v149, v91, v95 op_sel:[0,0,1]
	v_cvt_pk_fp8_f32 v150, v99, v103
	v_cvt_pk_fp8_f32 v150, v107, v111 op_sel:[0,0,1]
	v_cvt_pk_fp8_f32 v151, v115, v119
	v_cvt_pk_fp8_f32 v151, v123, v127 op_sel:[0,0,1]
	global_store_dwordx4 v153, v[148:151], s[34:35] offset:2048 sc1
	s_branch .LBB0_1050
